# P1 peeled first K-iteration: after the 16-store straight-line epilogue the first two DMA waits leave all 16 stores in flight (vmcnt(24)); vmcnt(16) kept after the general epilogue paths
# speedup vs baseline: 1.0018x; 1.0018x over previous
.LBB0_188:
	s_ashr_i32 s21, s20, 31
	s_lshl_b64 s[22:23], s[20:21], 20
	s_add_u32 s22, s31, s22
	s_addc_u32 s23, s34, s23
	s_and_b64 s[24:25], s[2:3], exec
	s_cselect_b32 s5, s23, s29
	s_cselect_b32 s7, s22, s28
	s_ashr_i32 s19, s18, 31
	s_lshl_b64 s[24:25], s[18:19], 20
	s_add_u32 s24, s35, s24
	s_addc_u32 s25, s36, s25
	s_and_b64 s[26:27], s[2:3], exec
	s_cselect_b32 s19, s25, s9
	s_cselect_b32 s21, s24, s8
	s_add_u32 s59, s8, 0x100
	s_addc_u32 s60, s9, 0
	s_add_u32 s8, s28, 0x80080
	v_mov_b32_e32 v0, 0
	s_addc_u32 s9, s29, 0
	s_mov_b32 s61, -2
	s_cmp_eq_u32 s56, 1
	s_cbranch_scc1 .Lpeel_zero_P1
	s_cmp_eq_u32 s101, 16
	s_cbranch_scc1 .Lpeel_alt_P1
	v_add_u32_e32 v140, s37, v193
	v_add_u32_e32 v160, s40, v193
	ds_read_b128 v[128:131], v140
	ds_read_b128 v[132:135], v140 offset:1024
	ds_read_b128 v[136:139], v140 offset:2048
	ds_read_b128 v[140:143], v140 offset:3072
	ds_read_b128 v[144:147], v160
	ds_read_b128 v[148:151], v160 offset:1024
	ds_read_b128 v[176:179], v160 offset:2048
	ds_read_b128 v[180:183], v160 offset:3072
	s_add_u32 s26, s8, 0xfff80080
	s_addc_u32 s27, s9, -1
	s_cmp_eq_u32 s61, 28
	s_cselect_b32 s29, s5, s27
	s_cselect_b32 s28, s7, s26
	s_cselect_b32 s27, s19, s60
	s_cselect_b32 s26, s21, s59
	v_lshl_add_u64 v[162:163], s[8:9], 0, v[174:175]
	s_add_i32 m0, s43, 0xc000
	ds_read_b128 v[184:187], v199
	ds_read_b128 v[188:191], v199 offset:1024
	ds_read_b128 v[200:203], v199 offset:2048
	ds_read_b128 v[204:207], v199 offset:3072
	ds_read_b128 v[208:211], v199 offset:4096
	ds_read_b128 v[212:215], v199 offset:5120
	ds_read_b128 v[216:219], v199 offset:6144
	ds_read_b128 v[230:233], v199 offset:7168
	global_load_lds_dwordx4 v[162:163], off
	v_lshl_add_u64 v[162:163], s[8:9], 0, v[172:173]
	s_add_i32 m0, s43, 0xe000
	s_nop 0
	global_load_lds_dwordx4 v[162:163], off
	s_waitcnt vmcnt(16)
	s_waitcnt lgkmcnt(0)
	s_barrier
	s_setprio 1
	s_waitcnt lgkmcnt(0)
	v_mfma_f32_16x16x32_bf16 v[124:127], v[128:131], v[184:187], 0
	v_mfma_f32_16x16x32_bf16 v[120:123], v[136:139], v[184:187], 0
	v_mfma_f32_16x16x32_bf16 v[108:111], v[128:131], v[200:203], 0
	v_mfma_f32_16x16x32_bf16 v[104:107], v[136:139], v[200:203], 0
	v_mfma_f32_16x16x32_bf16 v[92:95], v[128:131], v[208:211], 0
	v_mfma_f32_16x16x32_bf16 v[88:91], v[136:139], v[208:211], 0
	v_mfma_f32_16x16x32_bf16 v[76:79], v[128:131], v[216:219], 0
	v_mfma_f32_16x16x32_bf16 v[72:75], v[136:139], v[216:219], 0
	v_mfma_f32_16x16x32_bf16 v[124:127], v[132:135], v[188:191], v[124:127]
	v_mfma_f32_16x16x32_bf16 v[120:123], v[140:143], v[188:191], v[120:123]
	v_mfma_f32_16x16x32_bf16 v[108:111], v[132:135], v[204:207], v[108:111]
	v_mfma_f32_16x16x32_bf16 v[104:107], v[140:143], v[204:207], v[104:107]
	v_mfma_f32_16x16x32_bf16 v[92:95], v[132:135], v[212:215], v[92:95]
	v_mfma_f32_16x16x32_bf16 v[88:91], v[140:143], v[212:215], v[88:91]
	v_mfma_f32_16x16x32_bf16 v[76:79], v[132:135], v[230:233], v[76:79]
	v_mfma_f32_16x16x32_bf16 v[72:75], v[140:143], v[230:233], v[72:75]
	s_setprio 0
	s_setprio 1
	v_mfma_f32_16x16x32_bf16 v[116:119], v[144:147], v[184:187], 0
	v_mfma_f32_16x16x32_bf16 v[112:115], v[176:179], v[184:187], 0
	v_mfma_f32_16x16x32_bf16 v[100:103], v[144:147], v[200:203], 0
	v_mfma_f32_16x16x32_bf16 v[96:99], v[176:179], v[200:203], 0
	v_mfma_f32_16x16x32_bf16 v[84:87], v[144:147], v[208:211], 0
	v_mfma_f32_16x16x32_bf16 v[80:83], v[176:179], v[208:211], 0
	v_mfma_f32_16x16x32_bf16 v[68:71], v[144:147], v[216:219], 0
	v_mfma_f32_16x16x32_bf16 v[64:67], v[176:179], v[216:219], 0
	v_mfma_f32_16x16x32_bf16 v[116:119], v[148:151], v[188:191], v[116:119]
	v_mfma_f32_16x16x32_bf16 v[112:115], v[180:183], v[188:191], v[112:115]
	v_mfma_f32_16x16x32_bf16 v[100:103], v[148:151], v[204:207], v[100:103]
	v_mfma_f32_16x16x32_bf16 v[96:99], v[180:183], v[204:207], v[96:99]
	v_mfma_f32_16x16x32_bf16 v[84:87], v[148:151], v[212:215], v[84:87]
	v_mfma_f32_16x16x32_bf16 v[80:83], v[180:183], v[212:215], v[80:83]
	v_mfma_f32_16x16x32_bf16 v[68:71], v[148:151], v[230:233], v[68:71]
	v_mfma_f32_16x16x32_bf16 v[64:67], v[180:183], v[230:233], v[64:67]
	s_setprio 0
	s_barrier
	s_mov_b32 m0, s38
	v_lshl_add_u64 v[162:163], s[26:27], 0, v[154:155]
	s_add_u32 s62, s26, 0x80000
	ds_read_b128 v[184:187], v199 offset:16384
	ds_read_b128 v[188:191], v199 offset:17408
	ds_read_b128 v[200:203], v199 offset:18432
	ds_read_b128 v[204:207], v199 offset:19456
	ds_read_b128 v[208:211], v199 offset:20480
	ds_read_b128 v[212:215], v199 offset:21504
	ds_read_b128 v[216:219], v199 offset:22528
	ds_read_b128 v[230:233], v199 offset:23552
	global_load_lds_dwordx4 v[162:163], off
	v_lshl_add_u64 v[166:167], s[26:27], 0, v[158:159]
	s_mov_b32 m0, s39
	s_addc_u32 s63, s27, 0
	global_load_lds_dwordx4 v[166:167], off
	v_lshl_add_u64 v[194:195], s[62:63], 0, v[154:155]
	s_mov_b32 m0, s41
	v_lshl_add_u64 v[196:197], s[28:29], 0, v[156:157]
	global_load_lds_dwordx4 v[194:195], off
	v_lshl_add_u64 v[194:195], s[62:63], 0, v[158:159]
	s_mov_b32 m0, s42
	s_nop 0
	global_load_lds_dwordx4 v[194:195], off
	v_lshl_add_u64 v[194:195], s[28:29], 0, v[152:153]
	s_mov_b32 m0, s43
	s_nop 0
	global_load_lds_dwordx4 v[194:195], off
	s_mov_b32 m0, s44
	s_nop 0
	global_load_lds_dwordx4 v[196:197], off
	s_waitcnt vmcnt(16)
	s_waitcnt lgkmcnt(0)
	s_barrier
	s_setprio 1
	s_waitcnt lgkmcnt(0)
	v_mfma_f32_16x16x32_bf16 v[60:63], v[128:131], v[184:187], 0
	v_mfma_f32_16x16x32_bf16 v[56:59], v[136:139], v[184:187], 0
	v_mfma_f32_16x16x32_bf16 v[44:47], v[128:131], v[200:203], 0
	v_mfma_f32_16x16x32_bf16 v[40:43], v[136:139], v[200:203], 0
	v_mfma_f32_16x16x32_bf16 v[28:31], v[128:131], v[208:211], 0
	v_mfma_f32_16x16x32_bf16 v[24:27], v[136:139], v[208:211], 0
	v_mfma_f32_16x16x32_bf16 v[12:15], v[128:131], v[216:219], 0
	v_mfma_f32_16x16x32_bf16 v[8:11], v[136:139], v[216:219], 0
	v_mfma_f32_16x16x32_bf16 v[60:63], v[132:135], v[188:191], v[60:63]
	v_mfma_f32_16x16x32_bf16 v[56:59], v[140:143], v[188:191], v[56:59]
	v_mfma_f32_16x16x32_bf16 v[44:47], v[132:135], v[204:207], v[44:47]
	v_mfma_f32_16x16x32_bf16 v[40:43], v[140:143], v[204:207], v[40:43]
	v_mfma_f32_16x16x32_bf16 v[28:31], v[132:135], v[212:215], v[28:31]
	v_mfma_f32_16x16x32_bf16 v[24:27], v[140:143], v[212:215], v[24:27]
	v_mfma_f32_16x16x32_bf16 v[12:15], v[132:135], v[230:233], v[12:15]
	v_mfma_f32_16x16x32_bf16 v[8:11], v[140:143], v[230:233], v[8:11]
	s_setprio 0
	s_setprio 1
	v_mfma_f32_16x16x32_bf16 v[52:55], v[144:147], v[184:187], 0
	v_mfma_f32_16x16x32_bf16 v[48:51], v[176:179], v[184:187], 0
	v_mfma_f32_16x16x32_bf16 v[36:39], v[144:147], v[200:203], 0
	v_mfma_f32_16x16x32_bf16 v[32:35], v[176:179], v[200:203], 0
	v_mfma_f32_16x16x32_bf16 v[20:23], v[144:147], v[208:211], 0
	v_mfma_f32_16x16x32_bf16 v[16:19], v[176:179], v[208:211], 0
	v_mfma_f32_16x16x32_bf16 v[4:7], v[144:147], v[216:219], 0
	v_mfma_f32_16x16x32_bf16 v[0:3], v[176:179], v[216:219], 0
	v_mfma_f32_16x16x32_bf16 v[52:55], v[148:151], v[188:191], v[52:55]
	v_mfma_f32_16x16x32_bf16 v[48:51], v[180:183], v[188:191], v[48:51]
	v_mfma_f32_16x16x32_bf16 v[36:39], v[148:151], v[204:207], v[36:39]
	v_mfma_f32_16x16x32_bf16 v[32:35], v[180:183], v[204:207], v[32:35]
	v_mfma_f32_16x16x32_bf16 v[20:23], v[148:151], v[212:215], v[20:23]
	v_mfma_f32_16x16x32_bf16 v[16:19], v[180:183], v[212:215], v[16:19]
	v_mfma_f32_16x16x32_bf16 v[4:7], v[148:151], v[230:233], v[4:7]
	v_mfma_f32_16x16x32_bf16 v[0:3], v[180:183], v[230:233], v[0:3]
	s_setprio 0
	s_barrier
	v_add_u32_e32 v140, s48, v193
	v_add_u32_e32 v160, s53, v193
	ds_read_b128 v[128:131], v140
	ds_read_b128 v[132:135], v140 offset:1024
	ds_read_b128 v[136:139], v140 offset:2048
	ds_read_b128 v[140:143], v140 offset:3072
	ds_read_b128 v[144:147], v160
	ds_read_b128 v[148:151], v160 offset:1024
	ds_read_b128 v[176:179], v160 offset:2048
	ds_read_b128 v[180:183], v160 offset:3072
	s_add_u32 s28, s28, 0x80000
	s_addc_u32 s29, s29, 0
	s_mov_b32 m0, s45
	v_lshl_add_u64 v[220:221], s[28:29], 0, v[152:153]
	ds_read_b128 v[184:187], v199 offset:32768
	ds_read_b128 v[188:191], v199 offset:33792
	ds_read_b128 v[200:203], v199 offset:34816
	ds_read_b128 v[204:207], v199 offset:35840
	ds_read_b128 v[208:211], v199 offset:36864
	ds_read_b128 v[212:215], v199 offset:37888
	ds_read_b128 v[216:219], v199 offset:38912
	ds_read_b128 v[230:233], v199 offset:39936
	global_load_lds_dwordx4 v[220:221], off
	v_lshl_add_u64 v[220:221], s[28:29], 0, v[156:157]
	s_mov_b32 m0, s47
	s_nop 0
	global_load_lds_dwordx4 v[220:221], off
	s_waitcnt vmcnt(8)
	s_waitcnt lgkmcnt(0)
	s_barrier
	s_setprio 1
	s_waitcnt lgkmcnt(0)
	v_mfma_f32_16x16x32_bf16 v[124:127], v[128:131], v[184:187], v[124:127]
	v_mfma_f32_16x16x32_bf16 v[120:123], v[136:139], v[184:187], v[120:123]
	v_mfma_f32_16x16x32_bf16 v[108:111], v[128:131], v[200:203], v[108:111]
	v_mfma_f32_16x16x32_bf16 v[104:107], v[136:139], v[200:203], v[104:107]
	v_mfma_f32_16x16x32_bf16 v[92:95], v[128:131], v[208:211], v[92:95]
	v_mfma_f32_16x16x32_bf16 v[88:91], v[136:139], v[208:211], v[88:91]
	v_mfma_f32_16x16x32_bf16 v[76:79], v[128:131], v[216:219], v[76:79]
	v_mfma_f32_16x16x32_bf16 v[72:75], v[136:139], v[216:219], v[72:75]
	v_mfma_f32_16x16x32_bf16 v[124:127], v[132:135], v[188:191], v[124:127]
	v_mfma_f32_16x16x32_bf16 v[120:123], v[140:143], v[188:191], v[120:123]
	v_mfma_f32_16x16x32_bf16 v[108:111], v[132:135], v[204:207], v[108:111]
	v_mfma_f32_16x16x32_bf16 v[104:107], v[140:143], v[204:207], v[104:107]
	v_mfma_f32_16x16x32_bf16 v[92:95], v[132:135], v[212:215], v[92:95]
	v_mfma_f32_16x16x32_bf16 v[88:91], v[140:143], v[212:215], v[88:91]
	v_mfma_f32_16x16x32_bf16 v[76:79], v[132:135], v[230:233], v[76:79]
	v_mfma_f32_16x16x32_bf16 v[72:75], v[140:143], v[230:233], v[72:75]
	s_setprio 0
	s_setprio 1
	v_mfma_f32_16x16x32_bf16 v[116:119], v[144:147], v[184:187], v[116:119]
	v_mfma_f32_16x16x32_bf16 v[112:115], v[176:179], v[184:187], v[112:115]
	v_mfma_f32_16x16x32_bf16 v[100:103], v[144:147], v[200:203], v[100:103]
	v_mfma_f32_16x16x32_bf16 v[96:99], v[176:179], v[200:203], v[96:99]
	v_mfma_f32_16x16x32_bf16 v[84:87], v[144:147], v[208:211], v[84:87]
	v_mfma_f32_16x16x32_bf16 v[80:83], v[176:179], v[208:211], v[80:83]
	v_mfma_f32_16x16x32_bf16 v[68:71], v[144:147], v[216:219], v[68:71]
	v_mfma_f32_16x16x32_bf16 v[64:67], v[176:179], v[216:219], v[64:67]
	v_mfma_f32_16x16x32_bf16 v[116:119], v[148:151], v[188:191], v[116:119]
	v_mfma_f32_16x16x32_bf16 v[112:115], v[180:183], v[188:191], v[112:115]
	v_mfma_f32_16x16x32_bf16 v[100:103], v[148:151], v[204:207], v[100:103]
	v_mfma_f32_16x16x32_bf16 v[96:99], v[180:183], v[204:207], v[96:99]
	v_mfma_f32_16x16x32_bf16 v[84:87], v[148:151], v[212:215], v[84:87]
	v_mfma_f32_16x16x32_bf16 v[80:83], v[180:183], v[212:215], v[80:83]
	v_mfma_f32_16x16x32_bf16 v[68:71], v[148:151], v[230:233], v[68:71]
	v_mfma_f32_16x16x32_bf16 v[64:67], v[180:183], v[230:233], v[64:67]
	s_setprio 0
	s_barrier
	s_mov_b32 m0, s49
	v_lshl_add_u64 v[162:163], v[162:163], 0, s[86:87]
	s_add_u32 s26, s26, 0x80080
	ds_read_b128 v[184:187], v199 offset:49152
	ds_read_b128 v[188:191], v199 offset:50176
	ds_read_b128 v[200:203], v199 offset:51200
	ds_read_b128 v[204:207], v199 offset:52224
	ds_read_b128 v[208:211], v199 offset:53248
	ds_read_b128 v[212:215], v199 offset:54272
	ds_read_b128 v[216:219], v199 offset:55296
	ds_read_b128 v[230:233], v199 offset:56320
	global_load_lds_dwordx4 v[162:163], off
	v_lshl_add_u64 v[162:163], v[166:167], 0, s[86:87]
	s_mov_b32 m0, s50
	s_addc_u32 s27, s27, 0
	global_load_lds_dwordx4 v[162:163], off
	v_lshl_add_u64 v[162:163], s[26:27], 0, v[154:155]
	s_mov_b32 m0, s54
	s_nop 0
	global_load_lds_dwordx4 v[162:163], off
	v_lshl_add_u64 v[162:163], s[26:27], 0, v[158:159]
	s_mov_b32 m0, s55
	s_nop 0
	global_load_lds_dwordx4 v[162:163], off
	v_lshl_add_u64 v[162:163], v[194:195], 0, s[86:87]
	s_mov_b32 m0, s51
	s_nop 0
	global_load_lds_dwordx4 v[162:163], off
	v_lshl_add_u64 v[162:163], v[196:197], 0, s[86:87]
	s_mov_b32 m0, s52
	s_nop 0
	global_load_lds_dwordx4 v[162:163], off
	s_waitcnt vmcnt(8)
	s_waitcnt lgkmcnt(0)
	s_barrier
	s_setprio 1
	s_waitcnt lgkmcnt(0)
	v_mfma_f32_16x16x32_bf16 v[60:63], v[128:131], v[184:187], v[60:63]
	v_mfma_f32_16x16x32_bf16 v[56:59], v[136:139], v[184:187], v[56:59]
	v_mfma_f32_16x16x32_bf16 v[44:47], v[128:131], v[200:203], v[44:47]
	v_mfma_f32_16x16x32_bf16 v[40:43], v[136:139], v[200:203], v[40:43]
	v_mfma_f32_16x16x32_bf16 v[28:31], v[128:131], v[208:211], v[28:31]
	v_mfma_f32_16x16x32_bf16 v[24:27], v[136:139], v[208:211], v[24:27]
	v_mfma_f32_16x16x32_bf16 v[12:15], v[128:131], v[216:219], v[12:15]
	v_mfma_f32_16x16x32_bf16 v[8:11], v[136:139], v[216:219], v[8:11]
	v_mfma_f32_16x16x32_bf16 v[60:63], v[132:135], v[188:191], v[60:63]
	v_mfma_f32_16x16x32_bf16 v[56:59], v[140:143], v[188:191], v[56:59]
	v_mfma_f32_16x16x32_bf16 v[44:47], v[132:135], v[204:207], v[44:47]
	v_mfma_f32_16x16x32_bf16 v[40:43], v[140:143], v[204:207], v[40:43]
	v_mfma_f32_16x16x32_bf16 v[28:31], v[132:135], v[212:215], v[28:31]
	v_mfma_f32_16x16x32_bf16 v[24:27], v[140:143], v[212:215], v[24:27]
	v_mfma_f32_16x16x32_bf16 v[12:15], v[132:135], v[230:233], v[12:15]
	v_mfma_f32_16x16x32_bf16 v[8:11], v[140:143], v[230:233], v[8:11]
	s_setprio 0
	s_setprio 1
	v_mfma_f32_16x16x32_bf16 v[52:55], v[144:147], v[184:187], v[52:55]
	v_mfma_f32_16x16x32_bf16 v[48:51], v[176:179], v[184:187], v[48:51]
	v_mfma_f32_16x16x32_bf16 v[36:39], v[144:147], v[200:203], v[36:39]
	v_mfma_f32_16x16x32_bf16 v[32:35], v[176:179], v[200:203], v[32:35]
	v_mfma_f32_16x16x32_bf16 v[20:23], v[144:147], v[208:211], v[20:23]
	v_mfma_f32_16x16x32_bf16 v[16:19], v[176:179], v[208:211], v[16:19]
	v_mfma_f32_16x16x32_bf16 v[4:7], v[144:147], v[216:219], v[4:7]
	v_mfma_f32_16x16x32_bf16 v[0:3], v[176:179], v[216:219], v[0:3]
	v_mfma_f32_16x16x32_bf16 v[52:55], v[148:151], v[188:191], v[52:55]
	v_mfma_f32_16x16x32_bf16 v[48:51], v[180:183], v[188:191], v[48:51]
	v_mfma_f32_16x16x32_bf16 v[36:39], v[148:151], v[204:207], v[36:39]
	v_mfma_f32_16x16x32_bf16 v[32:35], v[180:183], v[204:207], v[32:35]
	v_mfma_f32_16x16x32_bf16 v[20:23], v[148:151], v[212:215], v[20:23]
	v_mfma_f32_16x16x32_bf16 v[16:19], v[180:183], v[212:215], v[16:19]
	v_mfma_f32_16x16x32_bf16 v[4:7], v[148:151], v[230:233], v[4:7]
	v_mfma_f32_16x16x32_bf16 v[0:3], v[180:183], v[230:233], v[0:3]
	s_setprio 0
	s_barrier
	s_add_i32 s61, s61, 2
	s_add_u32 s59, s59, 0x100
	s_addc_u32 s60, s60, 0
	s_add_u32 s8, s8, 0x100
	s_addc_u32 s9, s9, 0
	s_branch .LBB0_189
.Lpeel_alt_P1:
	v_add_u32_e32 v140, s37, v193
	v_add_u32_e32 v160, s40, v193
	ds_read_b128 v[128:131], v140
	ds_read_b128 v[132:135], v140 offset:1024
	ds_read_b128 v[136:139], v140 offset:2048
	ds_read_b128 v[140:143], v140 offset:3072
	ds_read_b128 v[144:147], v160
	ds_read_b128 v[148:151], v160 offset:1024
	ds_read_b128 v[176:179], v160 offset:2048
	ds_read_b128 v[180:183], v160 offset:3072
	s_add_u32 s26, s8, 0xfff80080
	s_addc_u32 s27, s9, -1
	s_cmp_eq_u32 s61, 28
	s_cselect_b32 s29, s5, s27
	s_cselect_b32 s28, s7, s26
	s_cselect_b32 s27, s19, s60
	s_cselect_b32 s26, s21, s59
	v_lshl_add_u64 v[162:163], s[8:9], 0, v[174:175]
	s_add_i32 m0, s43, 0xc000
	ds_read_b128 v[184:187], v199
	ds_read_b128 v[188:191], v199 offset:1024
	ds_read_b128 v[200:203], v199 offset:2048
	ds_read_b128 v[204:207], v199 offset:3072
	ds_read_b128 v[208:211], v199 offset:4096
	ds_read_b128 v[212:215], v199 offset:5120
	ds_read_b128 v[216:219], v199 offset:6144
	ds_read_b128 v[230:233], v199 offset:7168
	global_load_lds_dwordx4 v[162:163], off
	v_lshl_add_u64 v[162:163], s[8:9], 0, v[172:173]
	s_add_i32 m0, s43, 0xe000
	s_nop 0
	global_load_lds_dwordx4 v[162:163], off
	s_waitcnt vmcnt(24)
	s_waitcnt lgkmcnt(0)
	s_barrier
	s_setprio 1
	s_waitcnt lgkmcnt(0)
	v_mfma_f32_16x16x32_bf16 v[124:127], v[128:131], v[184:187], 0
	v_mfma_f32_16x16x32_bf16 v[120:123], v[136:139], v[184:187], 0
	v_mfma_f32_16x16x32_bf16 v[108:111], v[128:131], v[200:203], 0
	v_mfma_f32_16x16x32_bf16 v[104:107], v[136:139], v[200:203], 0
	v_mfma_f32_16x16x32_bf16 v[92:95], v[128:131], v[208:211], 0
	v_mfma_f32_16x16x32_bf16 v[88:91], v[136:139], v[208:211], 0
	v_mfma_f32_16x16x32_bf16 v[76:79], v[128:131], v[216:219], 0
	v_mfma_f32_16x16x32_bf16 v[72:75], v[136:139], v[216:219], 0
	v_mfma_f32_16x16x32_bf16 v[124:127], v[132:135], v[188:191], v[124:127]
	v_mfma_f32_16x16x32_bf16 v[120:123], v[140:143], v[188:191], v[120:123]
	v_mfma_f32_16x16x32_bf16 v[108:111], v[132:135], v[204:207], v[108:111]
	v_mfma_f32_16x16x32_bf16 v[104:107], v[140:143], v[204:207], v[104:107]
	v_mfma_f32_16x16x32_bf16 v[92:95], v[132:135], v[212:215], v[92:95]
	v_mfma_f32_16x16x32_bf16 v[88:91], v[140:143], v[212:215], v[88:91]
	v_mfma_f32_16x16x32_bf16 v[76:79], v[132:135], v[230:233], v[76:79]
	v_mfma_f32_16x16x32_bf16 v[72:75], v[140:143], v[230:233], v[72:75]
	s_setprio 0
	s_setprio 1
	v_mfma_f32_16x16x32_bf16 v[116:119], v[144:147], v[184:187], 0
	v_mfma_f32_16x16x32_bf16 v[112:115], v[176:179], v[184:187], 0
	v_mfma_f32_16x16x32_bf16 v[100:103], v[144:147], v[200:203], 0
	v_mfma_f32_16x16x32_bf16 v[96:99], v[176:179], v[200:203], 0
	v_mfma_f32_16x16x32_bf16 v[84:87], v[144:147], v[208:211], 0
	v_mfma_f32_16x16x32_bf16 v[80:83], v[176:179], v[208:211], 0
	v_mfma_f32_16x16x32_bf16 v[68:71], v[144:147], v[216:219], 0
	v_mfma_f32_16x16x32_bf16 v[64:67], v[176:179], v[216:219], 0
	v_mfma_f32_16x16x32_bf16 v[116:119], v[148:151], v[188:191], v[116:119]
	v_mfma_f32_16x16x32_bf16 v[112:115], v[180:183], v[188:191], v[112:115]
	v_mfma_f32_16x16x32_bf16 v[100:103], v[148:151], v[204:207], v[100:103]
	v_mfma_f32_16x16x32_bf16 v[96:99], v[180:183], v[204:207], v[96:99]
	v_mfma_f32_16x16x32_bf16 v[84:87], v[148:151], v[212:215], v[84:87]
	v_mfma_f32_16x16x32_bf16 v[80:83], v[180:183], v[212:215], v[80:83]
	v_mfma_f32_16x16x32_bf16 v[68:71], v[148:151], v[230:233], v[68:71]
	v_mfma_f32_16x16x32_bf16 v[64:67], v[180:183], v[230:233], v[64:67]
	s_setprio 0
	s_barrier
	s_mov_b32 m0, s38
	v_lshl_add_u64 v[162:163], s[26:27], 0, v[154:155]
	s_add_u32 s62, s26, 0x80000
	ds_read_b128 v[184:187], v199 offset:16384
	ds_read_b128 v[188:191], v199 offset:17408
	ds_read_b128 v[200:203], v199 offset:18432
	ds_read_b128 v[204:207], v199 offset:19456
	ds_read_b128 v[208:211], v199 offset:20480
	ds_read_b128 v[212:215], v199 offset:21504
	ds_read_b128 v[216:219], v199 offset:22528
	ds_read_b128 v[230:233], v199 offset:23552
	global_load_lds_dwordx4 v[162:163], off
	v_lshl_add_u64 v[166:167], s[26:27], 0, v[158:159]
	s_mov_b32 m0, s39
	s_addc_u32 s63, s27, 0
	global_load_lds_dwordx4 v[166:167], off
	v_lshl_add_u64 v[194:195], s[62:63], 0, v[154:155]
	s_mov_b32 m0, s41
	v_lshl_add_u64 v[196:197], s[28:29], 0, v[156:157]
	global_load_lds_dwordx4 v[194:195], off
	v_lshl_add_u64 v[194:195], s[62:63], 0, v[158:159]
	s_mov_b32 m0, s42
	s_nop 0
	global_load_lds_dwordx4 v[194:195], off
	v_lshl_add_u64 v[194:195], s[28:29], 0, v[152:153]
	s_mov_b32 m0, s43
	s_nop 0
	global_load_lds_dwordx4 v[194:195], off
	s_mov_b32 m0, s44
	s_nop 0
	global_load_lds_dwordx4 v[196:197], off
	s_waitcnt vmcnt(24)
	s_waitcnt lgkmcnt(0)
	s_barrier
	s_setprio 1
	s_waitcnt lgkmcnt(0)
	v_mfma_f32_16x16x32_bf16 v[60:63], v[128:131], v[184:187], 0
	v_mfma_f32_16x16x32_bf16 v[56:59], v[136:139], v[184:187], 0
	v_mfma_f32_16x16x32_bf16 v[44:47], v[128:131], v[200:203], 0
	v_mfma_f32_16x16x32_bf16 v[40:43], v[136:139], v[200:203], 0
	v_mfma_f32_16x16x32_bf16 v[28:31], v[128:131], v[208:211], 0
	v_mfma_f32_16x16x32_bf16 v[24:27], v[136:139], v[208:211], 0
	v_mfma_f32_16x16x32_bf16 v[12:15], v[128:131], v[216:219], 0
	v_mfma_f32_16x16x32_bf16 v[8:11], v[136:139], v[216:219], 0
	v_mfma_f32_16x16x32_bf16 v[60:63], v[132:135], v[188:191], v[60:63]
	v_mfma_f32_16x16x32_bf16 v[56:59], v[140:143], v[188:191], v[56:59]
	v_mfma_f32_16x16x32_bf16 v[44:47], v[132:135], v[204:207], v[44:47]
	v_mfma_f32_16x16x32_bf16 v[40:43], v[140:143], v[204:207], v[40:43]
	v_mfma_f32_16x16x32_bf16 v[28:31], v[132:135], v[212:215], v[28:31]
	v_mfma_f32_16x16x32_bf16 v[24:27], v[140:143], v[212:215], v[24:27]
	v_mfma_f32_16x16x32_bf16 v[12:15], v[132:135], v[230:233], v[12:15]
	v_mfma_f32_16x16x32_bf16 v[8:11], v[140:143], v[230:233], v[8:11]
	s_setprio 0
	s_setprio 1
	v_mfma_f32_16x16x32_bf16 v[52:55], v[144:147], v[184:187], 0
	v_mfma_f32_16x16x32_bf16 v[48:51], v[176:179], v[184:187], 0
	v_mfma_f32_16x16x32_bf16 v[36:39], v[144:147], v[200:203], 0
	v_mfma_f32_16x16x32_bf16 v[32:35], v[176:179], v[200:203], 0
	v_mfma_f32_16x16x32_bf16 v[20:23], v[144:147], v[208:211], 0
	v_mfma_f32_16x16x32_bf16 v[16:19], v[176:179], v[208:211], 0
	v_mfma_f32_16x16x32_bf16 v[4:7], v[144:147], v[216:219], 0
	v_mfma_f32_16x16x32_bf16 v[0:3], v[176:179], v[216:219], 0
	v_mfma_f32_16x16x32_bf16 v[52:55], v[148:151], v[188:191], v[52:55]
	v_mfma_f32_16x16x32_bf16 v[48:51], v[180:183], v[188:191], v[48:51]
	v_mfma_f32_16x16x32_bf16 v[36:39], v[148:151], v[204:207], v[36:39]
	v_mfma_f32_16x16x32_bf16 v[32:35], v[180:183], v[204:207], v[32:35]
	v_mfma_f32_16x16x32_bf16 v[20:23], v[148:151], v[212:215], v[20:23]
	v_mfma_f32_16x16x32_bf16 v[16:19], v[180:183], v[212:215], v[16:19]
	v_mfma_f32_16x16x32_bf16 v[4:7], v[148:151], v[230:233], v[4:7]
	v_mfma_f32_16x16x32_bf16 v[0:3], v[180:183], v[230:233], v[0:3]
	s_setprio 0
	s_barrier
	v_add_u32_e32 v140, s48, v193
	v_add_u32_e32 v160, s53, v193
	ds_read_b128 v[128:131], v140
	ds_read_b128 v[132:135], v140 offset:1024
	ds_read_b128 v[136:139], v140 offset:2048
	ds_read_b128 v[140:143], v140 offset:3072
	ds_read_b128 v[144:147], v160
	ds_read_b128 v[148:151], v160 offset:1024
	ds_read_b128 v[176:179], v160 offset:2048
	ds_read_b128 v[180:183], v160 offset:3072
	s_add_u32 s28, s28, 0x80000
	s_addc_u32 s29, s29, 0
	s_mov_b32 m0, s45
	v_lshl_add_u64 v[220:221], s[28:29], 0, v[152:153]
	ds_read_b128 v[184:187], v199 offset:32768
	ds_read_b128 v[188:191], v199 offset:33792
	ds_read_b128 v[200:203], v199 offset:34816
	ds_read_b128 v[204:207], v199 offset:35840
	ds_read_b128 v[208:211], v199 offset:36864
	ds_read_b128 v[212:215], v199 offset:37888
	ds_read_b128 v[216:219], v199 offset:38912
	ds_read_b128 v[230:233], v199 offset:39936
	global_load_lds_dwordx4 v[220:221], off
	v_lshl_add_u64 v[220:221], s[28:29], 0, v[156:157]
	s_mov_b32 m0, s47
	s_nop 0
	global_load_lds_dwordx4 v[220:221], off
	s_waitcnt vmcnt(8)
	s_waitcnt lgkmcnt(0)
	s_barrier
	s_setprio 1
	s_waitcnt lgkmcnt(0)
	v_mfma_f32_16x16x32_bf16 v[124:127], v[128:131], v[184:187], v[124:127]
	v_mfma_f32_16x16x32_bf16 v[120:123], v[136:139], v[184:187], v[120:123]
	v_mfma_f32_16x16x32_bf16 v[108:111], v[128:131], v[200:203], v[108:111]
	v_mfma_f32_16x16x32_bf16 v[104:107], v[136:139], v[200:203], v[104:107]
	v_mfma_f32_16x16x32_bf16 v[92:95], v[128:131], v[208:211], v[92:95]
	v_mfma_f32_16x16x32_bf16 v[88:91], v[136:139], v[208:211], v[88:91]
	v_mfma_f32_16x16x32_bf16 v[76:79], v[128:131], v[216:219], v[76:79]
	v_mfma_f32_16x16x32_bf16 v[72:75], v[136:139], v[216:219], v[72:75]
	v_mfma_f32_16x16x32_bf16 v[124:127], v[132:135], v[188:191], v[124:127]
	v_mfma_f32_16x16x32_bf16 v[120:123], v[140:143], v[188:191], v[120:123]
	v_mfma_f32_16x16x32_bf16 v[108:111], v[132:135], v[204:207], v[108:111]
	v_mfma_f32_16x16x32_bf16 v[104:107], v[140:143], v[204:207], v[104:107]
	v_mfma_f32_16x16x32_bf16 v[92:95], v[132:135], v[212:215], v[92:95]
	v_mfma_f32_16x16x32_bf16 v[88:91], v[140:143], v[212:215], v[88:91]
	v_mfma_f32_16x16x32_bf16 v[76:79], v[132:135], v[230:233], v[76:79]
	v_mfma_f32_16x16x32_bf16 v[72:75], v[140:143], v[230:233], v[72:75]
	s_setprio 0
	s_setprio 1
	v_mfma_f32_16x16x32_bf16 v[116:119], v[144:147], v[184:187], v[116:119]
	v_mfma_f32_16x16x32_bf16 v[112:115], v[176:179], v[184:187], v[112:115]
	v_mfma_f32_16x16x32_bf16 v[100:103], v[144:147], v[200:203], v[100:103]
	v_mfma_f32_16x16x32_bf16 v[96:99], v[176:179], v[200:203], v[96:99]
	v_mfma_f32_16x16x32_bf16 v[84:87], v[144:147], v[208:211], v[84:87]
	v_mfma_f32_16x16x32_bf16 v[80:83], v[176:179], v[208:211], v[80:83]
	v_mfma_f32_16x16x32_bf16 v[68:71], v[144:147], v[216:219], v[68:71]
	v_mfma_f32_16x16x32_bf16 v[64:67], v[176:179], v[216:219], v[64:67]
	v_mfma_f32_16x16x32_bf16 v[116:119], v[148:151], v[188:191], v[116:119]
	v_mfma_f32_16x16x32_bf16 v[112:115], v[180:183], v[188:191], v[112:115]
	v_mfma_f32_16x16x32_bf16 v[100:103], v[148:151], v[204:207], v[100:103]
	v_mfma_f32_16x16x32_bf16 v[96:99], v[180:183], v[204:207], v[96:99]
	v_mfma_f32_16x16x32_bf16 v[84:87], v[148:151], v[212:215], v[84:87]
	v_mfma_f32_16x16x32_bf16 v[80:83], v[180:183], v[212:215], v[80:83]
	v_mfma_f32_16x16x32_bf16 v[68:71], v[148:151], v[230:233], v[68:71]
	v_mfma_f32_16x16x32_bf16 v[64:67], v[180:183], v[230:233], v[64:67]
	s_setprio 0
	s_barrier
	s_mov_b32 m0, s49
	v_lshl_add_u64 v[162:163], v[162:163], 0, s[86:87]
	s_add_u32 s26, s26, 0x80080
	ds_read_b128 v[184:187], v199 offset:49152
	ds_read_b128 v[188:191], v199 offset:50176
	ds_read_b128 v[200:203], v199 offset:51200
	ds_read_b128 v[204:207], v199 offset:52224
	ds_read_b128 v[208:211], v199 offset:53248
	ds_read_b128 v[212:215], v199 offset:54272
	ds_read_b128 v[216:219], v199 offset:55296
	ds_read_b128 v[230:233], v199 offset:56320
	global_load_lds_dwordx4 v[162:163], off
	v_lshl_add_u64 v[162:163], v[166:167], 0, s[86:87]
	s_mov_b32 m0, s50
	s_addc_u32 s27, s27, 0
	global_load_lds_dwordx4 v[162:163], off
	v_lshl_add_u64 v[162:163], s[26:27], 0, v[154:155]
	s_mov_b32 m0, s54
	s_nop 0
	global_load_lds_dwordx4 v[162:163], off
	v_lshl_add_u64 v[162:163], s[26:27], 0, v[158:159]
	s_mov_b32 m0, s55
	s_nop 0
	global_load_lds_dwordx4 v[162:163], off
	v_lshl_add_u64 v[162:163], v[194:195], 0, s[86:87]
	s_mov_b32 m0, s51
	s_nop 0
	global_load_lds_dwordx4 v[162:163], off
	v_lshl_add_u64 v[162:163], v[196:197], 0, s[86:87]
	s_mov_b32 m0, s52
	s_nop 0
	global_load_lds_dwordx4 v[162:163], off
	s_waitcnt vmcnt(8)
	s_waitcnt lgkmcnt(0)
	s_barrier
	s_setprio 1
	s_waitcnt lgkmcnt(0)
	v_mfma_f32_16x16x32_bf16 v[60:63], v[128:131], v[184:187], v[60:63]
	v_mfma_f32_16x16x32_bf16 v[56:59], v[136:139], v[184:187], v[56:59]
	v_mfma_f32_16x16x32_bf16 v[44:47], v[128:131], v[200:203], v[44:47]
	v_mfma_f32_16x16x32_bf16 v[40:43], v[136:139], v[200:203], v[40:43]
	v_mfma_f32_16x16x32_bf16 v[28:31], v[128:131], v[208:211], v[28:31]
	v_mfma_f32_16x16x32_bf16 v[24:27], v[136:139], v[208:211], v[24:27]
	v_mfma_f32_16x16x32_bf16 v[12:15], v[128:131], v[216:219], v[12:15]
	v_mfma_f32_16x16x32_bf16 v[8:11], v[136:139], v[216:219], v[8:11]
	v_mfma_f32_16x16x32_bf16 v[60:63], v[132:135], v[188:191], v[60:63]
	v_mfma_f32_16x16x32_bf16 v[56:59], v[140:143], v[188:191], v[56:59]
	v_mfma_f32_16x16x32_bf16 v[44:47], v[132:135], v[204:207], v[44:47]
	v_mfma_f32_16x16x32_bf16 v[40:43], v[140:143], v[204:207], v[40:43]
	v_mfma_f32_16x16x32_bf16 v[28:31], v[132:135], v[212:215], v[28:31]
	v_mfma_f32_16x16x32_bf16 v[24:27], v[140:143], v[212:215], v[24:27]
	v_mfma_f32_16x16x32_bf16 v[12:15], v[132:135], v[230:233], v[12:15]
	v_mfma_f32_16x16x32_bf16 v[8:11], v[140:143], v[230:233], v[8:11]
	s_setprio 0
	s_setprio 1
	v_mfma_f32_16x16x32_bf16 v[52:55], v[144:147], v[184:187], v[52:55]
	v_mfma_f32_16x16x32_bf16 v[48:51], v[176:179], v[184:187], v[48:51]
	v_mfma_f32_16x16x32_bf16 v[36:39], v[144:147], v[200:203], v[36:39]
	v_mfma_f32_16x16x32_bf16 v[32:35], v[176:179], v[200:203], v[32:35]
	v_mfma_f32_16x16x32_bf16 v[20:23], v[144:147], v[208:211], v[20:23]
	v_mfma_f32_16x16x32_bf16 v[16:19], v[176:179], v[208:211], v[16:19]
	v_mfma_f32_16x16x32_bf16 v[4:7], v[144:147], v[216:219], v[4:7]
	v_mfma_f32_16x16x32_bf16 v[0:3], v[176:179], v[216:219], v[0:3]
	v_mfma_f32_16x16x32_bf16 v[52:55], v[148:151], v[188:191], v[52:55]
	v_mfma_f32_16x16x32_bf16 v[48:51], v[180:183], v[188:191], v[48:51]
	v_mfma_f32_16x16x32_bf16 v[36:39], v[148:151], v[204:207], v[36:39]
	v_mfma_f32_16x16x32_bf16 v[32:35], v[180:183], v[204:207], v[32:35]
	v_mfma_f32_16x16x32_bf16 v[20:23], v[148:151], v[212:215], v[20:23]
	v_mfma_f32_16x16x32_bf16 v[16:19], v[180:183], v[212:215], v[16:19]
	v_mfma_f32_16x16x32_bf16 v[4:7], v[148:151], v[230:233], v[4:7]
	v_mfma_f32_16x16x32_bf16 v[0:3], v[180:183], v[230:233], v[0:3]
	s_setprio 0
	s_barrier
	s_add_i32 s61, s61, 2
	s_add_u32 s59, s59, 0x100
	s_addc_u32 s60, s60, 0
	s_add_u32 s8, s8, 0x100
	s_addc_u32 s9, s9, 0
	s_branch .LBB0_189

.Lep_fast:
	s_mov_b32 s101, 16
	v_lshl_add_u32 v200, s4, 8, v192
	v_mov_b64_e32 v[202:203], s[10:11]
	s_lshl_b32 s98, s6, 8
	v_mad_i64_i32 v[202:203], vcc, v200, s84, v[202:203]
	v_or_b32_e32 v204, s98, v198
	v_mov_b32_e32 v205, 0
	v_lshl_add_u64 v[202:203], v[204:205], 1, v[202:203]
	s_mov_b32 s98, 0x68000
	s_mov_b32 s99, 0
	v_cvt_pk_bf16_f32 v208, v124, v125
	v_cvt_pk_bf16_f32 v209, v126, v127
	v_cvt_pk_bf16_f32 v210, v120, v121
	v_cvt_pk_bf16_f32 v211, v122, v123
	global_store_dwordx4 v[202:203], v[208:211], off nt
	v_cvt_pk_bf16_f32 v212, v116, v117
	v_cvt_pk_bf16_f32 v213, v118, v119
	v_cvt_pk_bf16_f32 v214, v112, v113
	v_cvt_pk_bf16_f32 v215, v114, v115
	global_store_dwordx4 v[202:203], v[212:215], off offset:256 nt
	v_lshl_add_u64 v[202:203], v[202:203], 0, s[98:99]
	v_cvt_pk_bf16_f32 v208, v108, v109
	v_cvt_pk_bf16_f32 v209, v110, v111
	v_cvt_pk_bf16_f32 v210, v104, v105
	v_cvt_pk_bf16_f32 v211, v106, v107
	global_store_dwordx4 v[202:203], v[208:211], off nt
	v_cvt_pk_bf16_f32 v212, v100, v101
	v_cvt_pk_bf16_f32 v213, v102, v103
	v_cvt_pk_bf16_f32 v214, v96, v97
	v_cvt_pk_bf16_f32 v215, v98, v99
	global_store_dwordx4 v[202:203], v[212:215], off offset:256 nt
	v_lshl_add_u64 v[202:203], v[202:203], 0, s[98:99]
	v_cvt_pk_bf16_f32 v208, v92, v93
	v_cvt_pk_bf16_f32 v209, v94, v95
	v_cvt_pk_bf16_f32 v210, v88, v89
	v_cvt_pk_bf16_f32 v211, v90, v91
	global_store_dwordx4 v[202:203], v[208:211], off nt
	v_cvt_pk_bf16_f32 v212, v84, v85
	v_cvt_pk_bf16_f32 v213, v86, v87
	v_cvt_pk_bf16_f32 v214, v80, v81
	v_cvt_pk_bf16_f32 v215, v82, v83
	global_store_dwordx4 v[202:203], v[212:215], off offset:256 nt
	v_lshl_add_u64 v[202:203], v[202:203], 0, s[98:99]
	v_cvt_pk_bf16_f32 v208, v76, v77
	v_cvt_pk_bf16_f32 v209, v78, v79
	v_cvt_pk_bf16_f32 v210, v72, v73
	v_cvt_pk_bf16_f32 v211, v74, v75
	global_store_dwordx4 v[202:203], v[208:211], off nt
	v_cvt_pk_bf16_f32 v212, v68, v69
	v_cvt_pk_bf16_f32 v213, v70, v71
	v_cvt_pk_bf16_f32 v214, v64, v65
	v_cvt_pk_bf16_f32 v215, v66, v67
	global_store_dwordx4 v[202:203], v[212:215], off offset:256 nt
	s_mov_b32 s98, 0x208000
	v_lshl_add_u64 v[202:203], v[202:203], 0, s[98:99]
	s_mov_b32 s98, 0x68000
	v_cvt_pk_bf16_f32 v208, v60, v61
	v_cvt_pk_bf16_f32 v209, v62, v63
	v_cvt_pk_bf16_f32 v210, v56, v57
	v_cvt_pk_bf16_f32 v211, v58, v59
	global_store_dwordx4 v[202:203], v[208:211], off nt
	v_cvt_pk_bf16_f32 v212, v52, v53
	v_cvt_pk_bf16_f32 v213, v54, v55
	v_cvt_pk_bf16_f32 v214, v48, v49
	v_cvt_pk_bf16_f32 v215, v50, v51
	global_store_dwordx4 v[202:203], v[212:215], off offset:256 nt
	v_lshl_add_u64 v[202:203], v[202:203], 0, s[98:99]
	v_cvt_pk_bf16_f32 v208, v44, v45
	v_cvt_pk_bf16_f32 v209, v46, v47
	v_cvt_pk_bf16_f32 v210, v40, v41
	v_cvt_pk_bf16_f32 v211, v42, v43
	global_store_dwordx4 v[202:203], v[208:211], off nt
	v_cvt_pk_bf16_f32 v212, v36, v37
	v_cvt_pk_bf16_f32 v213, v38, v39
	v_cvt_pk_bf16_f32 v214, v32, v33
	v_cvt_pk_bf16_f32 v215, v34, v35
	global_store_dwordx4 v[202:203], v[212:215], off offset:256 nt
	v_lshl_add_u64 v[202:203], v[202:203], 0, s[98:99]
	v_cvt_pk_bf16_f32 v208, v28, v29
	v_cvt_pk_bf16_f32 v209, v30, v31
	v_cvt_pk_bf16_f32 v210, v24, v25
	v_cvt_pk_bf16_f32 v211, v26, v27
	global_store_dwordx4 v[202:203], v[208:211], off nt
	v_cvt_pk_bf16_f32 v212, v20, v21
	v_cvt_pk_bf16_f32 v213, v22, v23
	v_cvt_pk_bf16_f32 v214, v16, v17
	v_cvt_pk_bf16_f32 v215, v18, v19
	global_store_dwordx4 v[202:203], v[212:215], off offset:256 nt
	v_lshl_add_u64 v[202:203], v[202:203], 0, s[98:99]
	v_cvt_pk_bf16_f32 v208, v12, v13
	v_cvt_pk_bf16_f32 v209, v14, v15
	v_cvt_pk_bf16_f32 v210, v8, v9
	v_cvt_pk_bf16_f32 v211, v10, v11
	global_store_dwordx4 v[202:203], v[208:211], off nt
	v_cvt_pk_bf16_f32 v212, v4, v5
	v_cvt_pk_bf16_f32 v213, v6, v7
	v_cvt_pk_bf16_f32 v214, v0, v1
	v_cvt_pk_bf16_f32 v215, v2, v3
	global_store_dwordx4 v[202:203], v[212:215], off offset:256 nt
	s_andn2_b64 vcc, exec, s[2:3]
	s_mov_b64 s[2:3], -1
	s_cbranch_vccnz .LBB0_185
	s_branch .LBB0_338
.Lep_slow:
	s_mov_b32 s101, 8
	v_lshl_add_u32 v176, s4, 8, v192
	s_add_i32 s4, s6, -12
	s_cmp_lt_u32 s4, 16
	s_cselect_b64 s[4:5], -1, 0
	s_and_b64 s[8:9], s[14:15], s[4:5]
	v_cndmask_b32_e64 v128, 0, 1, s[8:9]
	v_cmp_ne_u32_e64 s[4:5], 1, v128
	s_andn2_b64 vcc, exec, s[8:9]
	v_ashrrev_i32_e32 v177, 31, v176
	s_mov_b64 s[62:63], 0x100
	s_cbranch_vccnz .LBB0_194
	v_lshlrev_b64 v[128:129], 7, v[176:177]
	v_lshl_add_u64 v[128:129], v[170:171], 0, v[128:129]
	global_load_dwordx4 v[136:139], v[128:129], off
	global_load_dwordx4 v[140:143], v[128:129], off offset:64
	s_branch .LBB0_195
